# baseline (speedup 1.0000x reference)
_Z6k_attnPKDF16_PKfPDF16_:
	s_load_dwordx4 s[4:7], s[0:1], 0x0
	s_load_dwordx2 s[8:9], s[0:1], 0x10
	s_lshr_b32 s0, s2, 3
	s_sub_i32 s0, 0x2ff, s0
	s_lshl_b32 s1, s2, 5
	s_mul_hi_i32 s2, s0, 0x2aaaaaab
	s_lshr_b32 s3, s2, 31
	s_ashr_i32 s2, s2, 2
	s_and_b32 s1, s1, 0xe0
	s_add_i32 s2, s2, s3
	s_add_i32 s1, s2, s1
	s_mul_i32 s2, s2, 24
	s_sub_i32 s0, s0, s2
	s_mul_i32 s2, s0, 43
	s_bfe_u32 s3, s2, 0x1000f
	s_bfe_u32 s2, s2, 0x80008
	s_add_i32 s2, s2, s3
	s_sext_i32_i8 s2, s2
	s_mul_i32 s3, s2, -6
	s_add_i32 s3, s3, s0
	s_lshl_b32 s0, s1, 2
	s_add_i32 s2, s0, s2
	s_mul_i32 s1, s2, 0x48000
	s_mul_hi_i32 s0, s2, 0x48000
	s_waitcnt lgkmcnt(0)
	s_add_u32 s4, s4, s1
	s_addc_u32 s5, s5, s0
	s_lshl_b32 s0, s3, 7
	s_ashr_i32 s1, s0, 31
	s_lshl_b64 s[0:1], s[0:1], 1
	s_add_u32 s4, s4, s0
	v_lshlrev_b32_e32 v2, 4, v0
	v_lshrrev_b32_e32 v9, 4, v0
	s_addc_u32 s5, s5, s1
	v_and_b32_e32 v2, 0xf0, v2
	v_mov_b32_e32 v3, 0
	v_mul_u32_u24_e32 v6, 0x900, v9
	v_lshl_add_u64 v[4:5], s[4:5], 0, v[2:3]
	v_lshlrev_b32_e32 v6, 1, v6
	v_mov_b32_e32 v7, v3
	v_lshl_add_u64 v[6:7], v[4:5], 0, v[6:7]
	global_load_dwordx4 v[10:13], v[6:7], off offset:1536 nt
	global_load_dwordx4 v[14:17], v[6:7], off offset:3072 nt
	v_or_b32_e32 v6, 0x100, v0
	v_lshrrev_b32_e32 v50, 4, v6
	v_mul_u32_u24_e32 v6, 0x900, v50
	v_lshlrev_b32_e32 v6, 1, v6
	v_mov_b32_e32 v7, v3
	v_lshl_add_u64 v[6:7], v[4:5], 0, v[6:7]
	global_load_dwordx4 v[18:21], v[6:7], off offset:1536 nt
	global_load_dwordx4 v[22:25], v[6:7], off offset:3072 nt
	v_or_b32_e32 v6, 0x200, v0
	v_lshrrev_b32_e32 v51, 4, v6
	v_mul_u32_u24_e32 v6, 0x900, v51
	v_lshlrev_b32_e32 v6, 1, v6
	v_mov_b32_e32 v7, v3
	v_lshl_add_u64 v[6:7], v[4:5], 0, v[6:7]
	global_load_dwordx4 v[26:29], v[6:7], off offset:1536 nt
	global_load_dwordx4 v[30:33], v[6:7], off offset:3072 nt
	v_or_b32_e32 v6, 0x300, v0
	v_lshrrev_b32_e32 v52, 4, v6
	v_mul_u32_u24_e32 v6, 0x900, v52
	v_lshlrev_b32_e32 v6, 1, v6
	v_mov_b32_e32 v7, v3
	v_lshrrev_b32_e32 v1, 6, v0
	v_lshl_add_u64 v[4:5], v[4:5], 0, v[6:7]
	v_and_b32_e32 v8, 15, v0
	global_load_dwordx4 v[34:37], v[4:5], off offset:1536 nt
	global_load_dwordx4 v[38:41], v[4:5], off offset:3072 nt
	v_lshlrev_b32_e32 v6, 4, v1
	v_or_b32_e32 v4, v6, v8
	v_mul_u32_u24_e32 v4, 0x900, v4
	v_lshlrev_b32_e32 v4, 1, v4
	v_mov_b32_e32 v5, v3
	v_lshl_add_u64 v[4:5], s[4:5], 0, v[4:5]
	v_and_b32_e32 v58, 48, v0
	v_mov_b32_e32 v59, v3
	v_lshl_add_u64 v[4:5], v[4:5], 0, v[58:59]
	global_load_dwordx4 v[42:45], v[4:5], off nt
	global_load_dwordx4 v[46:49], v[4:5], off offset:64 nt
	s_movk_i32 s3, 0x110
	s_movk_i32 s4, 0x120
	v_or_b32_e32 v7, 0x4800, v2
	v_mad_u32_u24 v59, v9, s4, v2
	v_mad_u32_u24 v9, v9, s3, v7
	v_mad_u32_u24 v60, v50, s4, v2
	v_mad_u32_u24 v61, v51, s4, v2
	v_mad_u32_u24 v62, v52, s4, v2
	v_mad_u32_u24 v63, v50, s3, v7
	v_mad_u32_u24 v64, v51, s3, v7
	v_mad_u32_u24 v7, v52, s3, v7
	global_load_dwordx4 v[50:53], v[4:5], off offset:128 nt
	global_load_dwordx4 v[54:57], v[4:5], off offset:192 nt
	v_lshlrev_b32_e32 v4, 2, v8
	v_mov_b32_e32 v5, v3
	v_lshl_add_u64 v[4:5], s[6:7], 0, v[4:5]
	v_bfe_u32 v84, v0, 4, 2
	v_lshrrev_b32_e32 v85, 6, v0
	v_lshlrev_b32_e32 v84, 2, v84
	v_lshl_or_b32 v84, v85, 4, v84
	v_lshlrev_b32_e32 v84, 8, v84
	v_mov_b32_e32 v85, v3
	v_lshl_add_u64 v[84:85], v[4:5], 0, v[84:85]
	global_load_dword v68, v[84:85], off
	global_load_dword v69, v[84:85], off offset:64
	global_load_dword v70, v[84:85], off offset:128
	global_load_dword v71, v[84:85], off offset:192
	global_load_dword v72, v[84:85], off offset:256
	global_load_dword v73, v[84:85], off offset:320
	global_load_dword v74, v[84:85], off offset:384
	global_load_dword v75, v[84:85], off offset:448
	global_load_dword v76, v[84:85], off offset:512
	global_load_dword v77, v[84:85], off offset:576
	global_load_dword v78, v[84:85], off offset:640
	global_load_dword v79, v[84:85], off offset:704
	global_load_dword v80, v[84:85], off offset:768
	global_load_dword v81, v[84:85], off offset:832
	global_load_dword v82, v[84:85], off offset:896
	global_load_dword v83, v[84:85], off offset:960
	s_movk_i32 s4, 0x900
	s_waitcnt vmcnt(27)
	ds_write_b128 v9, v[10:13]
	s_waitcnt vmcnt(26)
	ds_write_b128 v59, v[14:17]
	s_waitcnt vmcnt(25)
	ds_write_b128 v63, v[18:21]
	s_waitcnt vmcnt(24)
	ds_write_b128 v60, v[22:25]
	s_waitcnt vmcnt(23)
	ds_write_b128 v64, v[26:29]
	s_waitcnt vmcnt(22)
	ds_write_b128 v61, v[30:33]
	s_waitcnt vmcnt(21)
	ds_write_b128 v7, v[34:37]
	s_waitcnt vmcnt(20)
	ds_write_b128 v62, v[38:41]
	v_mad_u32_u24 v30, v8, s3, v58
	s_waitcnt lgkmcnt(0)
	s_barrier
	ds_read_b128 v[10:13], v30 offset:18432
	ds_read_b128 v[14:17], v30 offset:18496
	s_waitcnt vmcnt(19) lgkmcnt(1)
	v_mfma_f32_16x16x32_f16 a[0:3], v[42:45], v[10:13], 0
	v_bfe_u32 v7, v0, 4, 2
	v_lshlrev_b32_e32 v9, 2, v7
	v_mbcnt_lo_u32_b32 v39, -1, 0
	s_waitcnt vmcnt(18) lgkmcnt(0)
	v_mfma_f32_16x16x32_f16 a[0:3], v[46:49], v[14:17], a[0:3]
	ds_read_b128 v[10:13], v30 offset:22784
	ds_read_b128 v[14:17], v30 offset:22848
	s_waitcnt lgkmcnt(1)
	v_mfma_f32_16x16x32_f16 a[4:7], v[42:45], v[10:13], 0
	s_waitcnt lgkmcnt(0)
	v_mfma_f32_16x16x32_f16 a[4:7], v[46:49], v[14:17], a[4:7]
	ds_read_b128 v[10:13], v30 offset:27136
	ds_read_b128 v[14:17], v30 offset:27200
	s_waitcnt lgkmcnt(1)
	v_mfma_f32_16x16x32_f16 a[8:11], v[42:45], v[10:13], 0
	ds_read_b128 v[10:13], v30 offset:31488
	s_waitcnt lgkmcnt(1)
	v_mfma_f32_16x16x32_f16 a[8:11], v[46:49], v[14:17], a[8:11]
	ds_read_b128 v[14:17], v30 offset:31552
	s_waitcnt lgkmcnt(1)
	v_mfma_f32_16x16x32_f16 a[12:15], v[42:45], v[10:13], 0
	v_or_b32_e32 v10, v9, v6
	v_lshlrev_b32_e32 v10, 8, v10
	v_mov_b32_e32 v11, v3
	v_lshl_add_u64 v[4:5], v[4:5], 0, v[10:11]
	s_waitcnt lgkmcnt(0)
	v_mfma_f32_16x16x32_f16 a[12:15], v[46:49], v[14:17], a[12:15]
	ds_read_b128 v[10:13], v30 offset:18560
	ds_read_b128 v[14:17], v30 offset:18624
	ds_read_b128 v[18:21], v30 offset:22912
	s_waitcnt vmcnt(17) lgkmcnt(2)
	v_mfma_f32_16x16x32_f16 a[0:3], v[50:53], v[10:13], a[0:3]
	ds_read_b128 v[10:13], v30 offset:22976
	ds_read_b128 v[22:25], v30 offset:27264
	ds_read_b128 v[26:29], v30 offset:27328
	s_waitcnt lgkmcnt(3)
	v_mfma_f32_16x16x32_f16 a[4:7], v[50:53], v[18:21], a[4:7]
	ds_read_b128 v[18:21], v30 offset:31616
	s_waitcnt lgkmcnt(2)
	v_mfma_f32_16x16x32_f16 a[8:11], v[50:53], v[22:25], a[8:11]
	ds_read_b128 v[22:25], v30 offset:31680
	s_waitcnt lgkmcnt(1)
	v_mfma_f32_16x16x32_f16 a[12:15], v[50:53], v[18:21], a[12:15]
	v_mbcnt_hi_u32_b32 v19, -1, v39
	v_lshlrev_b32_e32 v20, 3, v7
	v_lshlrev_b32_e32 v18, 3, v0
	s_waitcnt vmcnt(16)
	v_mfma_f32_16x16x32_f16 a[8:11], v[54:57], v[26:29], a[8:11]
	v_bfe_u32 v0, v0, 2, 2
	v_or_b32_e32 v0, v9, v0
	v_mul_u32_u24_e32 v0, 0x120, v0
	s_waitcnt lgkmcnt(0)
	v_mfma_f32_16x16x32_f16 a[12:15], v[54:57], v[22:25], a[12:15]
	v_and_or_b32 v0, v18, 24, v0
	v_mfma_f32_16x16x32_f16 a[0:3], v[54:57], v[14:17], a[0:3]
	v_and_b32_e32 v15, 64, v19
	v_xor_b32_e32 v14, 1, v19
	v_accvgpr_read_b32 v17, a8
	v_mfma_f32_16x16x32_f16 a[4:7], v[54:57], v[10:13], a[4:7]
	v_add_u32_e32 v12, 64, v15
	v_cmp_lt_i32_e32 vcc, v14, v12
	v_accvgpr_read_b32 v21, a12
	v_xor_b32_e32 v16, 2, v19
	v_cndmask_b32_e32 v13, v19, v14, vcc
	v_accvgpr_read_b32 v14, a0
	v_lshlrev_b32_e32 v13, 2, v13
	v_cmp_lt_i32_e32 vcc, v16, v12
	v_accvgpr_read_b32 v15, a4
	v_xor_b32_e32 v10, 4, v19
	v_cndmask_b32_e32 v16, v19, v16, vcc
	v_lshlrev_b32_e32 v16, 2, v16
	v_xor_b32_e32 v11, 8, v19
	v_cmp_lt_i32_e32 vcc, v10, v12
	v_accvgpr_read_b32 v26, a9
	v_accvgpr_read_b32 v22, a1
	v_cndmask_b32_e32 v10, v19, v10, vcc
	v_cmp_lt_i32_e32 vcc, v11, v12
	v_lshlrev_b32_e32 v10, 2, v10
	v_accvgpr_read_b32 v25, a5
	v_cndmask_b32_e32 v11, v19, v11, vcc
	v_lshlrev_b32_e32 v11, 2, v11
	v_accvgpr_read_b32 v41, a14
	v_accvgpr_read_b32 v23, a2
	v_accvgpr_read_b32 v42, a15
	v_accvgpr_read_b32 v24, a3
	s_waitcnt vmcnt(0)
	v_mov_b32_e32 v31, v68
	v_mov_b32_e32 v32, v69
	v_mov_b32_e32 v33, v70
	v_mov_b32_e32 v34, v71
	v_mov_b32_e32 v35, v72
	v_mov_b32_e32 v36, v73
	v_mov_b32_e32 v37, v74
	v_mov_b32_e32 v38, v75
	v_fmac_f32_e32 v31, 0x3e0293ee, v14
	s_waitcnt vmcnt(6)
	v_fmac_f32_e32 v32, 0x3e0293ee, v15
	s_waitcnt vmcnt(5)
	v_fmac_f32_e32 v33, 0x3e0293ee, v17
	s_waitcnt vmcnt(4)
	v_fmac_f32_e32 v34, 0x3e0293ee, v21
	v_max_f32_e32 v14, v33, v34
	v_max3_f32 v14, v31, v32, v14
	s_nop 1
	v_mov_b32_dpp v15, v14 quad_perm:[1,0,3,2] row_mask:0xf bank_mask:0xf
	s_waitcnt vmcnt(3)
	v_fmac_f32_e32 v35, 0x3e0293ee, v22
	s_waitcnt vmcnt(2)
	v_fmac_f32_e32 v36, 0x3e0293ee, v25
	s_waitcnt vmcnt(1)
	v_fmac_f32_e32 v37, 0x3e0293ee, v26
	s_waitcnt lgkmcnt(0)
	v_max_f32_e32 v15, v15, v15
	v_max_f32_e32 v14, v14, v15
	s_nop 1
	v_mov_b32_dpp v15, v14 quad_perm:[2,3,0,1] row_mask:0xf bank_mask:0xf
	s_waitcnt lgkmcnt(0)
	v_max_f32_e32 v12, v15, v15
	v_mov_b32_e32 v15, v76
	v_mov_b32_e32 v17, v77
	v_mov_b32_e32 v19, v78
	v_mov_b32_e32 v21, v79
	v_max_f32_e32 v12, v14, v12
	s_nop 1
	v_mov_b32_dpp v14, v12 row_half_mirror row_mask:0xf bank_mask:0xf
	s_waitcnt lgkmcnt(0)
	v_max_f32_e32 v14, v14, v14
	v_max_f32_e32 v12, v12, v14
	s_nop 1
	v_mov_b32_dpp v14, v12 row_mirror row_mask:0xf bank_mask:0xf
	s_waitcnt lgkmcnt(0)
	v_max_f32_e32 v14, v14, v14
	v_max_f32_e32 v12, v12, v14
	v_sub_f32_e32 v14, v31, v12
	v_sub_f32_e32 v27, v32, v12
	v_sub_f32_e32 v28, v33, v12
	v_sub_f32_e32 v12, v34, v12
	v_mov_b32_e32 v33, v80
	v_mov_b32_e32 v34, v81
	v_mov_b32_e32 v39, v82
	v_mov_b32_e32 v40, v83
	v_exp_f32_e32 v14, v14
	v_exp_f32_e32 v27, v27
	v_exp_f32_e32 v28, v28
	v_exp_f32_e32 v12, v12
	v_add_f32_e32 v29, 0, v14
	v_add_f32_e32 v29, v29, v27
	v_add_f32_e32 v29, v29, v28
	v_add_f32_e32 v29, v29, v12
	s_nop 1
	v_mov_b32_dpp v30, v29 quad_perm:[1,0,3,2] row_mask:0xf bank_mask:0xf
	v_accvgpr_read_b32 v31, a13
	s_waitcnt vmcnt(8)
	v_fmac_f32_e32 v38, 0x3e0293ee, v31
	v_max_f32_e32 v26, v37, v38
	v_max3_f32 v26, v35, v36, v26
	s_waitcnt lgkmcnt(0)
	v_add_f32_e32 v22, v29, v30
	s_nop 1
	v_mov_b32_dpp v29, v26 quad_perm:[1,0,3,2] row_mask:0xf bank_mask:0xf
	v_accvgpr_read_b32 v32, a10
	s_nop 1
	v_mov_b32_dpp v25, v22 quad_perm:[2,3,0,1] row_mask:0xf bank_mask:0xf
	v_accvgpr_read_b32 v30, a6
	v_accvgpr_read_b32 v4, a11
	s_waitcnt lgkmcnt(1)
	v_max_f32_e32 v29, v29, v29
	v_max_f32_e32 v26, v26, v29
	s_nop 1
	v_mov_b32_dpp v29, v26 quad_perm:[2,3,0,1] row_mask:0xf bank_mask:0xf
	s_waitcnt lgkmcnt(1)
	v_add_f32_e32 v22, v22, v25
	s_nop 1
	v_mov_b32_dpp v25, v22 row_half_mirror row_mask:0xf bank_mask:0xf
	v_accvgpr_read_b32 v31, a7
	v_cvt_f16_f32_e32 v14, v14
	s_waitcnt lgkmcnt(1)
	v_max_f32_e32 v5, v29, v29
	v_max_f32_e32 v5, v26, v5
	s_nop 1
	v_mov_b32_dpp v26, v5 row_half_mirror row_mask:0xf bank_mask:0xf
	s_waitcnt lgkmcnt(1)
	v_add_f32_e32 v22, v22, v25
	s_nop 1
	v_mov_b32_dpp v25, v22 row_mirror row_mask:0xf bank_mask:0xf
	v_cvt_f16_f32_e32 v27, v27
	v_cvt_f16_f32_e32 v28, v28
	s_waitcnt lgkmcnt(1)
	v_max_f32_e32 v26, v26, v26
	v_max_f32_e32 v5, v5, v26
	s_nop 1
	v_mov_b32_dpp v26, v5 row_mirror row_mask:0xf bank_mask:0xf
	s_waitcnt lgkmcnt(1)
	v_add_f32_e32 v22, v22, v25
	v_div_scale_f32 v25, s[6:7], v22, v22, 1.0
	v_rcp_f32_e32 v29, v25
	s_waitcnt lgkmcnt(0)
	v_max_f32_e32 v26, v26, v26
	v_max_f32_e32 v5, v5, v26
	v_sub_f32_e32 v26, v35, v5
	v_fma_f32 v43, -v25, v29, 1.0
	v_exp_f32_e32 v26, v26
	v_sub_f32_e32 v35, v36, v5
	v_fmac_f32_e32 v29, v43, v29
	v_exp_f32_e32 v35, v35
	v_sub_f32_e32 v36, v37, v5
	v_exp_f32_e32 v36, v36
	v_sub_f32_e32 v5, v38, v5
	v_exp_f32_e32 v5, v5
	v_add_f32_e32 v37, 0, v26
	v_add_f32_e32 v37, v37, v35
	v_add_f32_e32 v37, v37, v36
	v_add_f32_e32 v37, v37, v5
	s_waitcnt vmcnt(7)
	v_fmac_f32_e32 v15, 0x3e0293ee, v23
	s_waitcnt vmcnt(6)
	v_fmac_f32_e32 v17, 0x3e0293ee, v30
	s_waitcnt vmcnt(5)
	v_fmac_f32_e32 v19, 0x3e0293ee, v32
	s_waitcnt vmcnt(4)
	v_fmac_f32_e32 v21, 0x3e0293ee, v41
	v_max_f32_e32 v23, v19, v21
	v_max3_f32 v23, v15, v17, v23
	s_nop 1
	v_mov_b32_dpp v30, v23 quad_perm:[1,0,3,2] row_mask:0xf bank_mask:0xf
	v_div_scale_f32 v32, vcc, 1.0, v22, 1.0
	v_mul_f32_e32 v41, v32, v29
	v_fma_f32 v43, -v25, v41, v32
	s_waitcnt lgkmcnt(0)
	v_max_f32_e32 v30, v30, v30
	v_max_f32_e32 v23, v23, v30
	s_nop 1
	v_mov_b32_dpp v30, v23 quad_perm:[2,3,0,1] row_mask:0xf bank_mask:0xf
	v_fmac_f32_e32 v41, v43, v29
	v_fma_f32 v25, -v25, v41, v32
	v_div_fmas_f32 v25, v25, v29, v41
	s_nop 1
	v_mov_b32_dpp v38, v37 quad_perm:[1,0,3,2] row_mask:0xf bank_mask:0xf
	s_waitcnt lgkmcnt(1)
	v_max_f32_e32 v30, v30, v30
	v_max_f32_e32 v23, v23, v30
	s_nop 1
	v_mov_b32_dpp v30, v23 row_half_mirror row_mask:0xf bank_mask:0xf
	s_waitcnt vmcnt(3)
	v_fmac_f32_e32 v33, 0x3e0293ee, v24
	s_waitcnt vmcnt(1)
	v_fmac_f32_e32 v39, 0x3e0293ee, v4
	s_waitcnt vmcnt(0)
	v_fmac_f32_e32 v40, 0x3e0293ee, v42
	v_fmac_f32_e32 v34, 0x3e0293ee, v31
	s_waitcnt lgkmcnt(0)
	v_max_f32_e32 v30, v30, v30
	v_max_f32_e32 v23, v23, v30
	s_nop 1
	v_mov_b32_dpp v30, v23 row_mirror row_mask:0xf bank_mask:0xf
	v_max_f32_e32 v4, v39, v40
	v_max3_f32 v4, v33, v34, v4
	v_add_f32_e32 v37, v37, v38
	s_nop 1
	v_mov_b32_dpp v38, v37 quad_perm:[2,3,0,1] row_mask:0xf bank_mask:0xf
	s_waitcnt lgkmcnt(1)
	v_max_f32_e32 v29, v30, v30
	v_max_f32_e32 v23, v23, v29
	v_sub_f32_e32 v15, v15, v23
	v_sub_f32_e32 v17, v17, v23
	v_sub_f32_e32 v19, v19, v23
	v_sub_f32_e32 v21, v21, v23
	s_nop 1
	v_mov_b32_dpp v23, v4 quad_perm:[1,0,3,2] row_mask:0xf bank_mask:0xf
	s_waitcnt lgkmcnt(1)
	v_add_f32_e32 v37, v37, v38
	s_nop 1
	v_mov_b32_dpp v38, v37 row_half_mirror row_mask:0xf bank_mask:0xf
	v_exp_f32_e32 v15, v15
	v_exp_f32_e32 v17, v17
	s_waitcnt lgkmcnt(1)
	v_max_f32_e32 v23, v23, v23
	v_max_f32_e32 v4, v4, v23
	s_nop 1
	v_mov_b32_dpp v23, v4 quad_perm:[2,3,0,1] row_mask:0xf bank_mask:0xf
	s_waitcnt lgkmcnt(1)
	v_add_f32_e32 v32, v37, v38
	s_nop 1
	v_mov_b32_dpp v37, v32 row_mirror row_mask:0xf bank_mask:0xf
	v_div_fixup_f32 v22, v25, v22, 1.0
	v_exp_f32_e32 v19, v19
	s_waitcnt lgkmcnt(1)
	v_max_f32_e32 v23, v23, v23
	v_max_f32_e32 v4, v4, v23
	s_nop 1
	v_mov_b32_dpp v23, v4 row_half_mirror row_mask:0xf bank_mask:0xf
	s_waitcnt lgkmcnt(1)
	v_add_f32_e32 v25, v32, v37
	v_div_scale_f32 v29, s[6:7], v25, v25, 1.0
	v_exp_f32_e32 v21, v21
	s_waitcnt lgkmcnt(0)
	v_max_f32_e32 v23, v23, v23
	v_max_f32_e32 v4, v4, v23
	s_nop 1
	v_mov_b32_dpp v23, v4 row_mirror row_mask:0xf bank_mask:0xf
	v_rcp_f32_e32 v30, v29
	v_add_f32_e32 v32, 0, v15
	v_add_f32_e32 v24, v32, v17
	v_add_f32_e32 v24, v24, v19
	s_waitcnt lgkmcnt(0)
	v_max_f32_e32 v23, v23, v23
	v_max_f32_e32 v4, v4, v23
	v_add_f32_e32 v24, v24, v21
	v_sub_f32_e32 v23, v33, v4
	s_nop 1
	v_mov_b32_dpp v31, v24 quad_perm:[1,0,3,2] row_mask:0xf bank_mask:0xf
	v_fma_f32 v32, -v29, v30, 1.0
	v_exp_f32_e32 v23, v23
	v_sub_f32_e32 v33, v34, v4
	v_fmac_f32_e32 v30, v32, v30
	v_div_scale_f32 v32, vcc, 1.0, v25, 1.0
	v_exp_f32_e32 v33, v33
	v_sub_f32_e32 v34, v39, v4
	v_mul_f32_e32 v37, v32, v30
	v_exp_f32_e32 v34, v34
	v_sub_f32_e32 v4, v40, v4
	v_fma_f32 v38, -v29, v37, v32
	v_exp_f32_e32 v4, v4
	v_fmac_f32_e32 v37, v38, v30
	v_add_f32_e32 v38, 0, v23
	s_waitcnt lgkmcnt(0)
	v_add_f32_e32 v24, v24, v31
	v_add_f32_e32 v38, v38, v33
	s_nop 1
	v_mov_b32_dpp v31, v24 quad_perm:[2,3,0,1] row_mask:0xf bank_mask:0xf
	v_add_f32_e32 v38, v38, v34
	v_add_f32_e32 v38, v38, v4
	s_nop 1
	v_mov_b32_dpp v13, v38 quad_perm:[1,0,3,2] row_mask:0xf bank_mask:0xf
	v_fma_f32 v29, -v29, v37, v32
	s_waitcnt lgkmcnt(1)
	v_add_f32_e32 v24, v24, v31
	s_nop 1
	v_mov_b32_dpp v31, v24 row_half_mirror row_mask:0xf bank_mask:0xf
	v_div_fmas_f32 v29, v29, v30, v37
	s_waitcnt lgkmcnt(1)
	v_add_f32_e32 v13, v38, v13
	s_nop 1
	v_mov_b32_dpp v16, v13 quad_perm:[2,3,0,1] row_mask:0xf bank_mask:0xf
	v_div_fixup_f32 v25, v29, v25, 1.0
	s_waitcnt lgkmcnt(1)
	v_add_f32_e32 v24, v24, v31
	s_nop 1
	v_mov_b32_dpp v31, v24 row_mirror row_mask:0xf bank_mask:0xf
	v_cvt_f16_f32_e32 v12, v12
	s_waitcnt lgkmcnt(1)
	v_add_f32_e32 v13, v13, v16
	s_nop 1
	v_mov_b32_dpp v10, v13 row_half_mirror row_mask:0xf bank_mask:0xf
	v_cvt_f16_f32_e32 v26, v26
	s_waitcnt lgkmcnt(1)
	v_add_f32_e32 v24, v24, v31
	v_div_scale_f32 v30, s[6:7], v24, v24, 1.0
	v_rcp_f32_e32 v31, v30
	s_waitcnt lgkmcnt(0)
	v_add_f32_e32 v10, v13, v10
	s_nop 1
	v_mov_b32_dpp v11, v10 row_mirror row_mask:0xf bank_mask:0xf
	v_cvt_f16_f32_e32 v5, v5
	v_fma_f32 v16, -v30, v31, 1.0
	v_fmac_f32_e32 v31, v16, v31
	v_div_scale_f32 v16, vcc, 1.0, v24, 1.0
	v_mul_f32_e32 v13, v16, v31
	s_waitcnt lgkmcnt(0)
	v_add_f32_e32 v10, v10, v11
	v_fma_f32 v29, -v30, v13, v16
	v_div_scale_f32 v11, s[6:7], v10, v10, 1.0
	v_fmac_f32_e32 v13, v29, v31
	v_rcp_f32_e32 v29, v11
	v_fma_f32 v16, -v30, v13, v16
	v_div_fmas_f32 v13, v16, v31, v13
	v_div_fixup_f32 v13, v13, v24, 1.0
	v_fma_f32 v16, -v11, v29, 1.0
	v_fmac_f32_e32 v29, v16, v29
	v_mov_b32_e32 v16, 0x8c00
	v_mad_u32_u24 v16, v1, s4, v16
	v_lshlrev_b32_e32 v24, 1, v8
	v_or_b32_e32 v30, v16, v24
	s_movk_i32 s4, 0x240
	v_mad_u32_u24 v31, v7, s4, v30
	ds_write_b16 v31, v14
	ds_write_b16 v31, v27 offset:32
	ds_write_b16 v31, v28 offset:64
	ds_write_b16 v31, v12 offset:96
	v_cvt_f16_f32_e32 v27, v35
	v_or_b32_e32 v12, 1, v9
	s_movk_i32 s4, 0x90
	v_cvt_f16_f32_e32 v28, v36
	v_mad_u32_u24 v14, v12, s4, v30
	ds_write_b16 v14, v26
	ds_write_b16 v14, v27 offset:32
	ds_write_b16 v14, v28 offset:64
	ds_write_b16 v14, v5 offset:96
	v_cvt_f16_f32_e32 v5, v15
	v_cvt_f16_f32_e32 v15, v17
	v_cvt_f16_f32_e32 v17, v19
	v_cvt_f16_f32_e32 v19, v21
	ds_write_b16 v14, v5 offset:144
	ds_write_b16 v14, v15 offset:176
	ds_write_b16 v14, v17 offset:208
	ds_write_b16 v14, v19 offset:240
	v_cvt_f16_f32_e32 v5, v23
	v_cvt_f16_f32_e32 v15, v33
	v_cvt_f16_f32_e32 v17, v34
	v_cvt_f16_f32_e32 v4, v4
	ds_write_b16 v14, v5 offset:288
	ds_write_b16 v14, v15 offset:320
	ds_write_b16 v14, v17 offset:352
	ds_write_b16 v14, v4 offset:384
	v_mul_u32_u24_e32 v4, 0x90, v8
	v_add3_u32 v4, v16, v4, v20
	s_waitcnt lgkmcnt(0)
	s_barrier
	ds_read2_b64 v[36:39], v4 offset1:4
	ds_read2_b64 v[40:43], v4 offset0:8 offset1:12
	ds_read_b64_tr_b16 v[16:17], v0 offset:4608
	ds_read_b64_tr_b16 v[14:15], v0
	ds_read_b64_tr_b16 v[18:19], v0 offset:32
	ds_read_b64_tr_b16 v[30:31], v0 offset:64
	ds_read_b64_tr_b16 v[44:45], v0 offset:96
	ds_read_b64_tr_b16 v[20:21], v0 offset:4640
	ds_read_b64_tr_b16 v[32:33], v0 offset:4672
	ds_read_b64_tr_b16 v[46:47], v0 offset:4704
	s_waitcnt lgkmcnt(6)
	v_mfma_f32_16x16x32_f16 a[0:3], v[36:39], v[14:17], 0
	v_div_scale_f32 v4, vcc, 1.0, v10, 1.0
	v_mul_f32_e32 v5, v4, v29
	ds_read_b64_tr_b16 v[16:17], v0 offset:13824
	ds_read_b64_tr_b16 v[14:15], v0 offset:9216
	ds_read_b64_tr_b16 v[48:49], v0 offset:9248
	ds_read_b64_tr_b16 v[52:53], v0 offset:9280
	ds_read_b64_tr_b16 v[56:57], v0 offset:9312
	ds_read_b64_tr_b16 v[50:51], v0 offset:13856
	ds_read_b64_tr_b16 v[54:55], v0 offset:13888
	ds_read_b64_tr_b16 v[58:59], v0 offset:13920
	s_waitcnt lgkmcnt(6)
	v_mfma_f32_16x16x32_f16 a[0:3], v[40:43], v[14:17], a[0:3]
	v_fma_f32 v8, -v11, v5, v4
	v_fmac_f32_e32 v5, v8, v29
	v_fma_f32 v4, -v11, v5, v4
	v_mfma_f32_16x16x32_f16 a[4:7], v[36:39], v[18:21], 0
	v_div_fmas_f32 v4, v4, v29, v5
	v_div_fixup_f32 v4, v4, v10, 1.0
	s_movk_i32 s4, 0x1100
	v_mfma_f32_16x16x32_f16 a[8:11], v[36:39], v[30:33], 0
	v_accvgpr_read_b32 v5, a0
	v_accvgpr_read_b32 v8, a1
	v_accvgpr_read_b32 v9, a2
	s_waitcnt lgkmcnt(2)
	v_mfma_f32_16x16x32_f16 a[4:7], v[40:43], v[48:51], a[4:7]
	v_accvgpr_read_b32 v10, a3
	v_fma_mixlo_f16 v5, v5, v22, 0
	s_waitcnt lgkmcnt(1)
	v_mfma_f32_16x16x32_f16 a[0:3], v[40:43], v[52:55], a[8:11]
	v_mfma_f32_16x16x32_f16 a[8:11], v[36:39], v[44:47], 0
	ds_read_b64_tr_b16 v[28:29], v0 offset:4736
	ds_read_b64_tr_b16 v[26:27], v0 offset:128
	ds_read_b64_tr_b16 v[30:31], v0 offset:160
	ds_read_b64_tr_b16 v[44:45], v0 offset:192
	ds_read_b64_tr_b16 v[48:49], v0 offset:224
	ds_read_b64_tr_b16 v[32:33], v0 offset:4768
	ds_read_b64_tr_b16 v[46:47], v0 offset:4800
	ds_read_b64_tr_b16 v[50:51], v0 offset:4832
	v_accvgpr_read_b32 v11, a4
	v_accvgpr_read_b32 v14, a5
	v_accvgpr_read_b32 v15, a6
	v_accvgpr_read_b32 v16, a7
	v_accvgpr_read_b32 v17, a0
	v_accvgpr_read_b32 v18, a1
	s_waitcnt lgkmcnt(8)
	v_mfma_f32_16x16x32_f16 a[4:7], v[40:43], v[56:59], a[8:11]
	v_accvgpr_read_b32 v19, a3
	s_waitcnt lgkmcnt(6)
	v_mfma_f32_16x16x32_f16 a[8:11], v[36:39], v[26:29], 0
	ds_read_b64_tr_b16 v[28:29], v0 offset:13952
	ds_read_b64_tr_b16 v[26:27], v0 offset:9344
	ds_read_b64_tr_b16 v[52:53], v0 offset:9376
	ds_read_b64_tr_b16 v[56:57], v0 offset:9408
	ds_read_b64_tr_b16 v[60:61], v0 offset:9440
	ds_read_b64_tr_b16 v[54:55], v0 offset:13984
	ds_read_b64_tr_b16 v[58:59], v0 offset:14016
	ds_read_b64_tr_b16 v[62:63], v0 offset:14048
	v_accvgpr_read_b32 v0, a2
	v_accvgpr_read_b32 v20, a4
	s_waitcnt lgkmcnt(10)
	v_mfma_f32_16x16x32_f16 a[0:3], v[36:39], v[30:33], 0
	v_accvgpr_read_b32 v21, a5
	v_accvgpr_read_b32 v23, a6
	v_fma_mixlo_f16 v0, v0, v13, 0
	s_waitcnt lgkmcnt(2)
	v_mfma_f32_16x16x32_f16 a[0:3], v[40:43], v[52:55], a[0:3]
	v_mfma_f32_16x16x32_f16 a[8:11], v[40:43], v[26:29], a[8:11]
	v_accvgpr_read_b32 v26, a7
	v_mfma_f32_16x16x32_f16 a[4:7], v[36:39], v[44:47], 0
	s_nop 4
	v_accvgpr_read_b32 v31, a0
	v_accvgpr_read_b32 v32, a1
	v_accvgpr_read_b32 v33, a2
	v_accvgpr_read_b32 v34, a3
	v_mfma_f32_16x16x32_f16 a[0:3], v[36:39], v[48:51], 0
	v_accvgpr_read_b32 v27, a8
	v_accvgpr_read_b32 v28, a9
	v_accvgpr_read_b32 v29, a10
	s_waitcnt lgkmcnt(1)
	v_mfma_f32_16x16x32_f16 a[4:7], v[40:43], v[56:59], a[4:7]
	v_accvgpr_read_b32 v30, a11
	s_waitcnt lgkmcnt(0)
	v_mfma_f32_16x16x32_f16 a[0:3], v[40:43], v[60:63], a[0:3]
	v_mov_b32_e32 v43, 0x4800
	v_mad_u32_u24 v43, v1, s4, v43
	v_or_b32_e32 v1, v43, v24
	s_movk_i32 s4, 0x440
	v_mad_u32_u24 v24, v7, s4, v1
	ds_write_b16 v24, v5
	v_fma_mixlo_f16 v5, v8, v25, 0
	v_mad_u32_u24 v1, v12, s3, v1
	ds_write_b16 v1, v5
	v_fma_mixlo_f16 v5, v9, v13, 0
	ds_write_b16 v1, v5 offset:272
	v_fma_mixlo_f16 v5, v10, v4, 0
	ds_write_b16 v1, v5 offset:544
	v_fma_mixlo_f16 v5, v11, v22, 0
	ds_write_b16 v24, v5 offset:32
	v_fma_mixlo_f16 v5, v14, v25, 0
	ds_write_b16 v1, v5 offset:32
	v_fma_mixlo_f16 v5, v15, v13, 0
	ds_write_b16 v1, v5 offset:304
	v_fma_mixlo_f16 v5, v16, v4, 0
	ds_write_b16 v1, v5 offset:576
	v_fma_mixlo_f16 v5, v17, v22, 0
	ds_write_b16 v24, v5 offset:64
	ds_write_b16 v1, v0 offset:336
	v_fma_mixlo_f16 v0, v19, v4, 0
	v_fma_mixlo_f16 v5, v18, v25, 0
	ds_write_b16 v1, v0 offset:608
	v_fma_mixlo_f16 v0, v20, v22, 0
	ds_write_b16 v1, v5 offset:64
	ds_write_b16 v24, v0 offset:96
	v_fma_mixlo_f16 v0, v21, v25, 0
	ds_write_b16 v1, v0 offset:96
	v_fma_mixlo_f16 v0, v23, v13, 0
	ds_write_b16 v1, v0 offset:368
	v_fma_mixlo_f16 v0, v26, v4, 0
	ds_write_b16 v1, v0 offset:640
	v_fma_mixlo_f16 v0, v27, v22, 0
	ds_write_b16 v24, v0 offset:128
	v_fma_mixlo_f16 v0, v28, v25, 0
	ds_write_b16 v1, v0 offset:128
	v_fma_mixlo_f16 v0, v29, v13, 0
	ds_write_b16 v1, v0 offset:400
	v_fma_mixlo_f16 v0, v30, v4, 0
	ds_write_b16 v1, v0 offset:672
	v_fma_mixlo_f16 v0, v31, v22, 0
	ds_write_b16 v24, v0 offset:160
	v_fma_mixlo_f16 v0, v32, v25, 0
	ds_write_b16 v1, v0 offset:160
	v_fma_mixlo_f16 v0, v33, v13, 0
	v_accvgpr_read_b32 v35, a4
	ds_write_b16 v1, v0 offset:432
	v_fma_mixlo_f16 v0, v34, v4, 0
	v_accvgpr_read_b32 v36, a5
	ds_write_b16 v1, v0 offset:704
	v_fma_mixlo_f16 v0, v35, v22, 0
	v_accvgpr_read_b32 v37, a6
	ds_write_b16 v24, v0 offset:192
	v_fma_mixlo_f16 v0, v36, v25, 0
	v_accvgpr_read_b32 v38, a7
	ds_write_b16 v1, v0 offset:192
	v_fma_mixlo_f16 v0, v37, v13, 0
	v_accvgpr_read_b32 v39, a0
	ds_write_b16 v1, v0 offset:464
	v_fma_mixlo_f16 v0, v38, v4, 0
	v_accvgpr_read_b32 v40, a1
	ds_write_b16 v1, v0 offset:736
	v_fma_mixlo_f16 v0, v39, v22, 0
	v_accvgpr_read_b32 v41, a2
	ds_write_b16 v24, v0 offset:224
	v_fma_mixlo_f16 v0, v40, v25, 0
	v_accvgpr_read_b32 v42, a3
	ds_write_b16 v1, v0 offset:224
	v_fma_mixlo_f16 v0, v41, v13, 0
	ds_write_b16 v1, v0 offset:496
	v_fma_mixlo_f16 v0, v42, v4, 0
	ds_write_b16 v1, v0 offset:768
	v_lshl_or_b32 v4, s2, 6, v6
	s_movk_i32 s2, 0x600
	v_mov_b64_e32 v[0:1], s[8:9]
	v_mad_i64_i32 v[0:1], s[4:5], v4, s2, v[0:1]
	v_lshl_add_u64 v[0:1], v[0:1], 0, s[0:1]
	v_or_b32_e32 v4, v43, v2
	v_lshl_add_u64 v[0:1], v[0:1], 0, v[2:3]
	v_mul_u32_u24_e32 v2, 0x300, v7
	v_mad_u32_u24 v6, v7, s3, v4
	v_lshlrev_b32_e32 v2, 1, v2
	s_waitcnt lgkmcnt(0)
	ds_read_b128 v[8:11], v6
	v_lshl_add_u64 v[12:13], v[0:1], 0, v[2:3]
	ds_read_b128 v[0:3], v6 offset:1088
	s_movk_i32 s0, 0x1000
	v_add_co_u32_e32 v4, vcc, s0, v12
	s_waitcnt lgkmcnt(1)
	global_store_dwordx4 v[12:13], v[8:11], off nt
	v_addc_co_u32_e32 v5, vcc, 0, v13, vcc
	s_waitcnt lgkmcnt(0)
	global_store_dwordx4 v[4:5], v[0:3], off offset:2048 nt
	ds_read_b128 v[0:3], v6 offset:2176
	ds_read_b128 v[4:7], v6 offset:3264
	v_add_co_u32_e32 v8, vcc, 0x3000, v12
	s_nop 1
	v_addc_co_u32_e32 v9, vcc, 0, v13, vcc
	s_waitcnt lgkmcnt(1)
	global_store_dwordx4 v[8:9], v[0:3], off nt
	s_nop 1
	v_add_co_u32_e32 v0, vcc, 0x4000, v12
	s_nop 1
	v_addc_co_u32_e32 v1, vcc, 0, v13, vcc
	s_waitcnt lgkmcnt(0)
	global_store_dwordx4 v[0:1], v[4:7], off offset:2048 nt
	s_endpgm

	.amdhsa_kernel _Z6k_attnPKDF16_PKfPDF16_
		.amdhsa_group_segment_fixed_size 45056
		.amdhsa_private_segment_fixed_size 0
		.amdhsa_kernarg_size 24
		.amdhsa_user_sgpr_count 2
		.amdhsa_user_sgpr_dispatch_ptr 0
		.amdhsa_user_sgpr_queue_ptr 0
		.amdhsa_user_sgpr_kernarg_segment_ptr 1
		.amdhsa_user_sgpr_dispatch_id 0
		.amdhsa_user_sgpr_kernarg_preload_length 0
		.amdhsa_user_sgpr_kernarg_preload_offset 0
		.amdhsa_user_sgpr_private_segment_size 0
		.amdhsa_uses_dynamic_stack 0
		.amdhsa_enable_private_segment 0
		.amdhsa_system_sgpr_workgroup_id_x 1
		.amdhsa_system_sgpr_workgroup_id_y 0
		.amdhsa_system_sgpr_workgroup_id_z 0
		.amdhsa_system_sgpr_workgroup_info 0
		.amdhsa_system_vgpr_workitem_id 0
		.amdhsa_next_free_vgpr 129
		.amdhsa_next_free_sgpr 96
		.amdhsa_accum_offset 88
		.amdhsa_reserve_vcc 1
		.amdhsa_float_round_mode_32 0
		.amdhsa_float_round_mode_16_64 0
		.amdhsa_float_denorm_mode_32 3
		.amdhsa_float_denorm_mode_16_64 3
		.amdhsa_dx10_clamp 1
		.amdhsa_ieee_mode 1
		.amdhsa_fp16_overflow 0
		.amdhsa_tg_split 0
		.amdhsa_exception_fp_ieee_invalid_op 0
		.amdhsa_exception_fp_denorm_src 0
		.amdhsa_exception_fp_ieee_div_zero 0
		.amdhsa_exception_fp_ieee_overflow 0
		.amdhsa_exception_fp_ieee_underflow 0
		.amdhsa_exception_fp_ieee_inexact 0
		.amdhsa_exception_int_div_zero 0
	.end_amdhsa_kernel

amdhsa.kernels:
  - .agpr_count:     16
    .args:
      - .actual_access:  read_only
        .address_space:  global
        .offset:         0
        .size:           8
        .value_kind:     global_buffer
      - .actual_access:  read_only
        .address_space:  global
        .offset:         8
        .size:           8
        .value_kind:     global_buffer
      - .actual_access:  write_only
        .address_space:  global
        .offset:         16
        .size:           8
        .value_kind:     global_buffer
    .group_segment_fixed_size: 45056
    .kernarg_segment_align: 8
    .kernarg_segment_size: 24
    .language:       OpenCL C
    .language_version:
      - 2
      - 0
    .max_flat_workgroup_size: 256
    .name:           _Z6k_attnPKDF16_PKfPDF16_
    .private_segment_fixed_size: 0
    .sgpr_count:     16
    .sgpr_spill_count: 0
    .symbol:         _Z6k_attnPKDF16_PKfPDF16_.kd
    .uniform_work_group_size: 1
    .uses_dynamic_stack: false
    .vgpr_count:     104
    .vgpr_spill_count: 0
    .wavefront_size: 64
  - .agpr_count:     0
    .args:
      - .actual_access:  read_only
        .address_space:  global
        .offset:         0
        .size:           8
        .value_kind:     global_buffer
      - .actual_access:  read_only
        .address_space:  global
        .offset:         8
        .size:           8
        .value_kind:     global_buffer
      - .actual_access:  write_only
        .address_space:  global
        .offset:         16
        .size:           8
        .value_kind:     global_buffer
      - .actual_access:  write_only
        .address_space:  global
        .offset:         24
        .size:           8
        .value_kind:     global_buffer
      - .actual_access:  write_only
        .address_space:  global
        .offset:         32
        .size:           8
        .value_kind:     global_buffer
      - .actual_access:  write_only
        .address_space:  global
        .offset:         40
        .size:           8
        .value_kind:     global_buffer
    .group_segment_fixed_size: 0
    .kernarg_segment_align: 8
    .kernarg_segment_size: 48
    .language:       OpenCL C
    .language_version:
      - 2
      - 0
    .max_flat_workgroup_size: 256
    .name:           _Z11k_prep_miscPKiPKfPfPDv2_fS3_S3_
    .private_segment_fixed_size: 0
    .sgpr_count:     16
    .sgpr_spill_count: 0
    .symbol:         _Z11k_prep_miscPKiPKfPfPDv2_fS3_S3_.kd
    .uniform_work_group_size: 1
    .uses_dynamic_stack: false
    .vgpr_count:     6
    .vgpr_spill_count: 0
    .wavefront_size: 64
  - .agpr_count:     0
    .args:
      - .actual_access:  read_only
        .address_space:  global
        .offset:         0
        .size:           8
        .value_kind:     global_buffer
      - .actual_access:  write_only
        .address_space:  global
        .offset:         8
        .size:           8
        .value_kind:     global_buffer
    .group_segment_fixed_size: 0
    .kernarg_segment_align: 8
    .kernarg_segment_size: 16
    .language:       OpenCL C
    .language_version:
      - 2
      - 0
    .max_flat_workgroup_size: 256
    .name:           _Z7k_cvt_xPKfPDF16_
    .private_segment_fixed_size: 0
    .sgpr_count:     14
    .sgpr_spill_count: 0
    .symbol:         _Z7k_cvt_xPKfPDF16_.kd
    .uniform_work_group_size: 1
    .uses_dynamic_stack: false
    .vgpr_count:     12
    .vgpr_spill_count: 0
    .wavefront_size: 64
  - .agpr_count:     0
    .args:
      - .offset:         0
        .size:           176
        .value_kind:     by_value
    .group_segment_fixed_size: 9216
    .kernarg_segment_align: 8
    .kernarg_segment_size: 176
    .language:       OpenCL C
    .language_version:
      - 2
      - 0
    .max_flat_workgroup_size: 256
    .name:           _Z8k_wtrans8PrepArgs
    .private_segment_fixed_size: 0
    .sgpr_count:     44
    .sgpr_spill_count: 0
    .symbol:         _Z8k_wtrans8PrepArgs.kd
    .uniform_work_group_size: 1
    .uses_dynamic_stack: false
    .vgpr_count:     18
    .vgpr_spill_count: 0
    .wavefront_size: 64
  - .agpr_count:     0
    .args:
      - .offset:         0
        .size:           176
        .value_kind:     by_value
      - .actual_access:  read_only
        .address_space:  global
        .offset:         176
        .size:           8
        .value_kind:     global_buffer
      - .actual_access:  read_only
        .address_space:  global
        .offset:         184
        .size:           8
        .value_kind:     global_buffer
    .group_segment_fixed_size: 2048
    .kernarg_segment_align: 8
    .kernarg_segment_size: 192
    .language:       OpenCL C
    .language_version:
      - 2
      - 0
    .max_flat_workgroup_size: 256
    .name:           _Z8k_colvec8PrepArgsPKfS1_
    .private_segment_fixed_size: 0
    .sgpr_count:     38
    .sgpr_spill_count: 0
    .symbol:         _Z8k_colvec8PrepArgsPKfS1_.kd
    .uniform_work_group_size: 1
    .uses_dynamic_stack: false
    .vgpr_count:     114
    .vgpr_spill_count: 0
    .wavefront_size: 64
  - .agpr_count:     0
    .args:
      - .actual_access:  read_only
        .address_space:  global
        .offset:         0
        .size:           8
        .value_kind:     global_buffer
      - .actual_access:  write_only
        .address_space:  global
        .offset:         8
        .size:           8
        .value_kind:     global_buffer
    .group_segment_fixed_size: 0
    .kernarg_segment_align: 8
    .kernarg_segment_size: 16
    .language:       OpenCL C
    .language_version:
      - 2
      - 0
    .max_flat_workgroup_size: 256
    .name:           _Z9k_rowstatPKDv2_fPS_
    .private_segment_fixed_size: 0
    .sgpr_count:     16
    .sgpr_spill_count: 0
    .symbol:         _Z9k_rowstatPKDv2_fPS_.kd
    .uniform_work_group_size: 1
    .uses_dynamic_stack: false
    .vgpr_count:     28
    .vgpr_spill_count: 0
    .wavefront_size: 64
  - .agpr_count:     0
    .args:
      - .actual_access:  read_only
        .address_space:  global
        .offset:         0
        .size:           8
        .value_kind:     global_buffer
      - .actual_access:  read_only
        .address_space:  global
        .offset:         8
        .size:           8
        .value_kind:     global_buffer
      - .actual_access:  read_only
        .address_space:  global
        .offset:         16
        .size:           8
        .value_kind:     global_buffer
      - .actual_access:  read_only
        .address_space:  global
        .offset:         24
        .size:           8
        .value_kind:     global_buffer
      - .actual_access:  write_only
        .address_space:  global
        .offset:         32
        .size:           8
        .value_kind:     global_buffer
    .group_segment_fixed_size: 0
    .kernarg_segment_align: 8
    .kernarg_segment_size: 40
    .language:       OpenCL C
    .language_version:
      - 2
      - 0
    .max_flat_workgroup_size: 256
    .name:           _Z10k_final_lnPKDF16_PKDv2_fPKfS5_Pf
    .private_segment_fixed_size: 0
    .sgpr_count:     19
    .sgpr_spill_count: 0
    .symbol:         _Z10k_final_lnPKDF16_PKDv2_fPKfS5_Pf.kd
    .uniform_work_group_size: 1
    .uses_dynamic_stack: false
    .vgpr_count:     19
    .vgpr_spill_count: 0
    .wavefront_size: 64
  - .agpr_count:     0
    .args:
      - .offset:         0
        .size:           32
        .value_kind:     by_value
      - .offset:         32
        .size:           32
        .value_kind:     by_value
      - .offset:         64
        .size:           4
        .value_kind:     hidden_block_count_x
      - .offset:         68
        .size:           4
        .value_kind:     hidden_block_count_y
      - .offset:         72
        .size:           4
        .value_kind:     hidden_block_count_z
      - .offset:         76
        .size:           2
        .value_kind:     hidden_group_size_x
      - .offset:         78
        .size:           2
        .value_kind:     hidden_group_size_y
      - .offset:         80
        .size:           2
        .value_kind:     hidden_group_size_z
      - .offset:         82
        .size:           2
        .value_kind:     hidden_remainder_x
      - .offset:         84
        .size:           2
        .value_kind:     hidden_remainder_y
      - .offset:         86
        .size:           2
        .value_kind:     hidden_remainder_z
      - .offset:         104
        .size:           8
        .value_kind:     hidden_global_offset_x
      - .offset:         112
        .size:           8
        .value_kind:     hidden_global_offset_y
      - .offset:         120
        .size:           8
        .value_kind:     hidden_global_offset_z
      - .offset:         128
        .size:           2
        .value_kind:     hidden_grid_dims
      - .offset:         184
        .size:           4
        .value_kind:     hidden_dynamic_lds_size
    .group_segment_fixed_size: 0
    .kernarg_segment_align: 8
    .kernarg_segment_size: 320
    .language:       OpenCL C
    .language_version:
      - 2
      - 0
    .max_flat_workgroup_size: 512
    .name:           _Z6k_gemmIN2pg6EpiLinILi0EEELi768EEvNS0_4GemmET_
    .private_segment_fixed_size: 0
    .sgpr_count:     88
    .sgpr_spill_count: 0
    .symbol:         _Z6k_gemmIN2pg6EpiLinILi0EEELi768EEvNS0_4GemmET_.kd
    .uniform_work_group_size: 1
    .uses_dynamic_stack: false
    .vgpr_count:     254
    .vgpr_spill_count: 0
    .wavefront_size: 64
  - .agpr_count:     0
    .args:
      - .offset:         0
        .size:           32
        .value_kind:     by_value
      - .offset:         32
        .size:           56
        .value_kind:     by_value
      - .offset:         88
        .size:           4
        .value_kind:     hidden_block_count_x
      - .offset:         92
        .size:           4
        .value_kind:     hidden_block_count_y
      - .offset:         96
        .size:           4
        .value_kind:     hidden_block_count_z
      - .offset:         100
        .size:           2
        .value_kind:     hidden_group_size_x
      - .offset:         102
        .size:           2
        .value_kind:     hidden_group_size_y
      - .offset:         104
        .size:           2
        .value_kind:     hidden_group_size_z
      - .offset:         106
        .size:           2
        .value_kind:     hidden_remainder_x
      - .offset:         108
        .size:           2
        .value_kind:     hidden_remainder_y
      - .offset:         110
        .size:           2
        .value_kind:     hidden_remainder_z
      - .offset:         128
        .size:           8
        .value_kind:     hidden_global_offset_x
      - .offset:         136
        .size:           8
        .value_kind:     hidden_global_offset_y
      - .offset:         144
        .size:           8
        .value_kind:     hidden_global_offset_z
      - .offset:         152
        .size:           2
        .value_kind:     hidden_grid_dims
      - .offset:         208
        .size:           4
        .value_kind:     hidden_dynamic_lds_size
    .group_segment_fixed_size: 0
    .kernarg_segment_align: 8
    .kernarg_segment_size: 344
    .language:       OpenCL C
    .language_version:
      - 2
      - 0
    .max_flat_workgroup_size: 512
    .name:           _Z6k_gemmIN2pg6EpiResELi768EEvNS0_4GemmET_
    .private_segment_fixed_size: 0
    .sgpr_count:     108
    .sgpr_spill_count: 0
    .symbol:         _Z6k_gemmIN2pg6EpiResELi768EEvNS0_4GemmET_.kd
    .uniform_work_group_size: 1
    .uses_dynamic_stack: false
    .vgpr_count:     256
    .vgpr_spill_count: 0
    .wavefront_size: 64
  - .agpr_count:     0
    .args:
      - .offset:         0
        .size:           32
        .value_kind:     by_value
      - .offset:         32
        .size:           32
        .value_kind:     by_value
      - .offset:         64
        .size:           4
        .value_kind:     hidden_block_count_x
      - .offset:         68
        .size:           4
        .value_kind:     hidden_block_count_y
      - .offset:         72
        .size:           4
        .value_kind:     hidden_block_count_z
      - .offset:         76
        .size:           2
        .value_kind:     hidden_group_size_x
      - .offset:         78
        .size:           2
        .value_kind:     hidden_group_size_y
      - .offset:         80
        .size:           2
        .value_kind:     hidden_group_size_z
      - .offset:         82
        .size:           2
        .value_kind:     hidden_remainder_x
      - .offset:         84
        .size:           2
        .value_kind:     hidden_remainder_y
      - .offset:         86
        .size:           2
        .value_kind:     hidden_remainder_z
      - .offset:         104
        .size:           8
        .value_kind:     hidden_global_offset_x
      - .offset:         112
        .size:           8
        .value_kind:     hidden_global_offset_y
      - .offset:         120
        .size:           8
        .value_kind:     hidden_global_offset_z
      - .offset:         128
        .size:           2
        .value_kind:     hidden_grid_dims
      - .offset:         184
        .size:           4
        .value_kind:     hidden_dynamic_lds_size
    .group_segment_fixed_size: 0
    .kernarg_segment_align: 8
    .kernarg_segment_size: 320
    .language:       OpenCL C
    .language_version:
      - 2
      - 0
    .max_flat_workgroup_size: 512
    .name:           _Z6k_gemmIN2pg6EpiLinILi1EEELi768EEvNS0_4GemmET_
    .private_segment_fixed_size: 0
    .sgpr_count:     88
    .sgpr_spill_count: 0
    .symbol:         _Z6k_gemmIN2pg6EpiLinILi1EEELi768EEvNS0_4GemmET_.kd
    .uniform_work_group_size: 1
    .uses_dynamic_stack: false
    .vgpr_count:     254
    .vgpr_spill_count: 0
    .wavefront_size: 64
  - .agpr_count:     0
    .args:
      - .offset:         0
        .size:           32
        .value_kind:     by_value
      - .offset:         32
        .size:           56
        .value_kind:     by_value
      - .offset:         88
        .size:           4
        .value_kind:     hidden_block_count_x
      - .offset:         92
        .size:           4
        .value_kind:     hidden_block_count_y
      - .offset:         96
        .size:           4
        .value_kind:     hidden_block_count_z
      - .offset:         100
        .size:           2
        .value_kind:     hidden_group_size_x
      - .offset:         102
        .size:           2
        .value_kind:     hidden_group_size_y
      - .offset:         104
        .size:           2
        .value_kind:     hidden_group_size_z
      - .offset:         106
        .size:           2
        .value_kind:     hidden_remainder_x
      - .offset:         108
        .size:           2
        .value_kind:     hidden_remainder_y
      - .offset:         110
        .size:           2
        .value_kind:     hidden_remainder_z
      - .offset:         128
        .size:           8
        .value_kind:     hidden_global_offset_x
      - .offset:         136
        .size:           8
        .value_kind:     hidden_global_offset_y
      - .offset:         144
        .size:           8
        .value_kind:     hidden_global_offset_z
      - .offset:         152
        .size:           2
        .value_kind:     hidden_grid_dims
      - .offset:         208
        .size:           4
        .value_kind:     hidden_dynamic_lds_size
    .group_segment_fixed_size: 0
    .kernarg_segment_align: 8
    .kernarg_segment_size: 344
    .language:       OpenCL C
    .language_version:
      - 2
      - 0
    .max_flat_workgroup_size: 512
    .name:           _Z6k_gemmIN2pg6EpiResELi3072EEvNS0_4GemmET_
    .private_segment_fixed_size: 0
    .sgpr_count:     108
    .sgpr_spill_count: 0
    .symbol:         _Z6k_gemmIN2pg6EpiResELi3072EEvNS0_4GemmET_.kd
    .uniform_work_group_size: 1
    .uses_dynamic_stack: false
    .vgpr_count:     256
    .vgpr_spill_count: 0
    .wavefront_size: 64
